# P3 residual epilogue: two rounds of base loads in flight with counted vmcnt (was four load->vmcnt(0)->add->store rounds); stacked on peeled K-loops
# baseline (speedup 1.0000x reference)
.Lpeel_528_after:
	v_lshl_add_u32 v186, s46, 8, v148
	v_lshl_or_b32 v142, s47, 8, v150
	v_ashrrev_i32_e32 v143, 31, v142
	v_or_b32_e32 v170, 16, v186
	v_lshlrev_b64 v[146:147], 2, v[142:143]
	v_ashrrev_i32_e32 v187, 31, v186
	v_ashrrev_i32_e32 v171, 31, v170
	v_lshl_add_u64 v[142:143], s[68:69], 0, v[146:147]
	v_lshlrev_b64 v[144:145], 13, v[186:187]
	v_lshlrev_b64 v[188:189], 13, v[170:171]
	v_lshl_add_u64 v[166:167], v[142:143], 0, v[144:145]
	v_lshl_add_u64 v[182:183], v[142:143], 0, v[188:189]
	v_lshl_add_u64 v[220:221], s[50:51], 0, v[146:147]
	v_lshl_add_u64 v[218:219], v[142:143], 0, v[144:145]
	v_lshl_add_u64 v[220:221], v[220:221], 0, v[144:145]
	global_load_dwordx4 v[154:157], v[218:219], off
	global_load_dwordx4 v[158:161], v[218:219], off offset:64
	global_load_dwordx4 v[162:165], v[218:219], off offset:512
	global_load_dwordx4 v[166:169], v[218:219], off offset:576
	v_add_co_u32_e32 v222, vcc, 0x20000, v218
	s_nop 1
	v_addc_co_u32_e32 v223, vcc, 0, v219, vcc
	global_load_dwordx4 v[170:173], v[222:223], off
	global_load_dwordx4 v[174:177], v[222:223], off offset:64
	global_load_dwordx4 v[178:181], v[222:223], off offset:512
	global_load_dwordx4 v[182:185], v[222:223], off offset:576
	v_add_co_u32_e32 v222, vcc, 0x40000, v218
	s_nop 1
	v_addc_co_u32_e32 v223, vcc, 0, v219, vcc
	global_load_dwordx4 v[186:189], v[222:223], off
	global_load_dwordx4 v[190:193], v[222:223], off offset:64
	global_load_dwordx4 v[194:197], v[222:223], off offset:512
	global_load_dwordx4 v[198:201], v[222:223], off offset:576
	v_add_co_u32_e32 v222, vcc, 0x60000, v218
	s_nop 1
	v_addc_co_u32_e32 v223, vcc, 0, v219, vcc
	global_load_dwordx4 v[202:205], v[222:223], off
	global_load_dwordx4 v[206:209], v[222:223], off offset:64
	global_load_dwordx4 v[210:213], v[222:223], off offset:512
	global_load_dwordx4 v[214:217], v[222:223], off offset:576
	s_waitcnt vmcnt(8)
	v_pk_add_f32 v[126:127], v[126:127], v[154:155]
	v_pk_add_f32 v[128:129], v[128:129], v[156:157]
	v_pk_add_f32 v[122:123], v[122:123], v[158:159]
	v_pk_add_f32 v[124:125], v[124:125], v[160:161]
	v_pk_add_f32 v[110:111], v[110:111], v[162:163]
	v_pk_add_f32 v[112:113], v[112:113], v[164:165]
	v_pk_add_f32 v[106:107], v[106:107], v[166:167]
	v_pk_add_f32 v[108:109], v[108:109], v[168:169]
	v_pk_add_f32 v[118:119], v[118:119], v[170:171]
	v_pk_add_f32 v[120:121], v[120:121], v[172:173]
	v_pk_add_f32 v[114:115], v[114:115], v[174:175]
	v_pk_add_f32 v[116:117], v[116:117], v[176:177]
	v_pk_add_f32 v[102:103], v[102:103], v[178:179]
	v_pk_add_f32 v[104:105], v[104:105], v[180:181]
	v_pk_add_f32 v[98:99], v[98:99], v[182:183]
	v_pk_add_f32 v[100:101], v[100:101], v[184:185]
	global_store_dwordx4 v[220:221], v[126:129], off
	global_store_dwordx4 v[220:221], v[122:125], off offset:64
	global_store_dwordx4 v[220:221], v[110:113], off offset:512
	global_store_dwordx4 v[220:221], v[106:109], off offset:576
	v_add_co_u32_e32 v224, vcc, 0x20000, v220
	s_nop 1
	v_addc_co_u32_e32 v225, vcc, 0, v221, vcc
	global_store_dwordx4 v[224:225], v[118:121], off
	global_store_dwordx4 v[224:225], v[114:117], off offset:64
	global_store_dwordx4 v[224:225], v[102:105], off offset:512
	global_store_dwordx4 v[224:225], v[98:101], off offset:576
	v_add_co_u32_e32 v222, vcc, 0x100000, v218
	s_nop 1
	v_addc_co_u32_e32 v223, vcc, 0, v219, vcc
	global_load_dwordx4 v[154:157], v[222:223], off
	global_load_dwordx4 v[158:161], v[222:223], off offset:64
	global_load_dwordx4 v[162:165], v[222:223], off offset:512
	global_load_dwordx4 v[166:169], v[222:223], off offset:576
	v_add_co_u32_e32 v222, vcc, 0x120000, v218
	s_nop 1
	v_addc_co_u32_e32 v223, vcc, 0, v219, vcc
	global_load_dwordx4 v[170:173], v[222:223], off
	global_load_dwordx4 v[174:177], v[222:223], off offset:64
	global_load_dwordx4 v[178:181], v[222:223], off offset:512
	global_load_dwordx4 v[182:185], v[222:223], off offset:576
	s_waitcnt vmcnt(16)
	v_pk_add_f32 v[94:95], v[94:95], v[186:187]
	v_pk_add_f32 v[96:97], v[96:97], v[188:189]
	v_pk_add_f32 v[90:91], v[90:91], v[190:191]
	v_pk_add_f32 v[92:93], v[92:93], v[192:193]
	v_pk_add_f32 v[78:79], v[78:79], v[194:195]
	v_pk_add_f32 v[80:81], v[80:81], v[196:197]
	v_pk_add_f32 v[74:75], v[74:75], v[198:199]
	v_pk_add_f32 v[76:77], v[76:77], v[200:201]
	v_pk_add_f32 v[86:87], v[86:87], v[202:203]
	v_pk_add_f32 v[88:89], v[88:89], v[204:205]
	v_pk_add_f32 v[82:83], v[82:83], v[206:207]
	v_pk_add_f32 v[84:85], v[84:85], v[208:209]
	v_pk_add_f32 v[70:71], v[70:71], v[210:211]
	v_pk_add_f32 v[72:73], v[72:73], v[212:213]
	v_pk_add_f32 v[66:67], v[66:67], v[214:215]
	v_pk_add_f32 v[68:69], v[68:69], v[216:217]
	v_add_co_u32_e32 v224, vcc, 0x40000, v220
	s_nop 1
	v_addc_co_u32_e32 v225, vcc, 0, v221, vcc
	global_store_dwordx4 v[224:225], v[94:97], off
	global_store_dwordx4 v[224:225], v[90:93], off offset:64
	global_store_dwordx4 v[224:225], v[78:81], off offset:512
	global_store_dwordx4 v[224:225], v[74:77], off offset:576
	v_add_co_u32_e32 v224, vcc, 0x60000, v220
	s_nop 1
	v_addc_co_u32_e32 v225, vcc, 0, v221, vcc
	global_store_dwordx4 v[224:225], v[86:89], off
	global_store_dwordx4 v[224:225], v[82:85], off offset:64
	global_store_dwordx4 v[224:225], v[70:73], off offset:512
	global_store_dwordx4 v[224:225], v[66:69], off offset:576
	v_add_co_u32_e32 v222, vcc, 0x140000, v218
	s_nop 1
	v_addc_co_u32_e32 v223, vcc, 0, v219, vcc
	global_load_dwordx4 v[186:189], v[222:223], off
	global_load_dwordx4 v[190:193], v[222:223], off offset:64
	global_load_dwordx4 v[194:197], v[222:223], off offset:512
	global_load_dwordx4 v[198:201], v[222:223], off offset:576
	v_add_co_u32_e32 v222, vcc, 0x160000, v218
	s_nop 1
	v_addc_co_u32_e32 v223, vcc, 0, v219, vcc
	global_load_dwordx4 v[202:205], v[222:223], off
	global_load_dwordx4 v[206:209], v[222:223], off offset:64
	global_load_dwordx4 v[210:213], v[222:223], off offset:512
	global_load_dwordx4 v[214:217], v[222:223], off offset:576
	s_waitcnt vmcnt(16)
	v_pk_add_f32 v[62:63], v[62:63], v[154:155]
	v_pk_add_f32 v[64:65], v[64:65], v[156:157]
	v_pk_add_f32 v[58:59], v[58:59], v[158:159]
	v_pk_add_f32 v[60:61], v[60:61], v[160:161]
	v_pk_add_f32 v[46:47], v[46:47], v[162:163]
	v_pk_add_f32 v[48:49], v[48:49], v[164:165]
	v_pk_add_f32 v[42:43], v[42:43], v[166:167]
	v_pk_add_f32 v[44:45], v[44:45], v[168:169]
	v_pk_add_f32 v[54:55], v[54:55], v[170:171]
	v_pk_add_f32 v[56:57], v[56:57], v[172:173]
	v_pk_add_f32 v[50:51], v[50:51], v[174:175]
	v_pk_add_f32 v[52:53], v[52:53], v[176:177]
	v_pk_add_f32 v[38:39], v[38:39], v[178:179]
	v_pk_add_f32 v[40:41], v[40:41], v[180:181]
	v_pk_add_f32 v[34:35], v[34:35], v[182:183]
	v_pk_add_f32 v[36:37], v[36:37], v[184:185]
	v_add_co_u32_e32 v224, vcc, 0x100000, v220
	s_nop 1
	v_addc_co_u32_e32 v225, vcc, 0, v221, vcc
	global_store_dwordx4 v[224:225], v[62:65], off
	global_store_dwordx4 v[224:225], v[58:61], off offset:64
	global_store_dwordx4 v[224:225], v[46:49], off offset:512
	global_store_dwordx4 v[224:225], v[42:45], off offset:576
	v_add_co_u32_e32 v224, vcc, 0x120000, v220
	s_nop 1
	v_addc_co_u32_e32 v225, vcc, 0, v221, vcc
	global_store_dwordx4 v[224:225], v[54:57], off
	global_store_dwordx4 v[224:225], v[50:53], off offset:64
	global_store_dwordx4 v[224:225], v[38:41], off offset:512
	global_store_dwordx4 v[224:225], v[34:37], off offset:576
	s_waitcnt vmcnt(8)
	v_pk_add_f32 v[30:31], v[30:31], v[186:187]
	v_pk_add_f32 v[32:33], v[32:33], v[188:189]
	v_pk_add_f32 v[26:27], v[26:27], v[190:191]
	v_pk_add_f32 v[28:29], v[28:29], v[192:193]
	v_pk_add_f32 v[14:15], v[14:15], v[194:195]
	v_pk_add_f32 v[16:17], v[16:17], v[196:197]
	v_pk_add_f32 v[10:11], v[10:11], v[198:199]
	v_pk_add_f32 v[12:13], v[12:13], v[200:201]
	v_pk_add_f32 v[22:23], v[22:23], v[202:203]
	v_pk_add_f32 v[24:25], v[24:25], v[204:205]
	v_pk_add_f32 v[18:19], v[18:19], v[206:207]
	v_pk_add_f32 v[20:21], v[20:21], v[208:209]
	v_pk_add_f32 v[6:7], v[6:7], v[210:211]
	v_pk_add_f32 v[8:9], v[8:9], v[212:213]
	v_pk_add_f32 v[2:3], v[2:3], v[214:215]
	v_pk_add_f32 v[4:5], v[4:5], v[216:217]
	v_add_co_u32_e32 v224, vcc, 0x140000, v220
	s_nop 1
	v_addc_co_u32_e32 v225, vcc, 0, v221, vcc
	global_store_dwordx4 v[224:225], v[30:33], off
	global_store_dwordx4 v[224:225], v[26:29], off offset:64
	global_store_dwordx4 v[224:225], v[14:17], off offset:512
	global_store_dwordx4 v[224:225], v[10:13], off offset:576
	v_add_co_u32_e32 v224, vcc, 0x160000, v220
	s_nop 1
	v_addc_co_u32_e32 v225, vcc, 0, v221, vcc
	global_store_dwordx4 v[224:225], v[22:25], off
	global_store_dwordx4 v[224:225], v[18:21], off offset:64
	global_store_dwordx4 v[224:225], v[6:9], off offset:512
	global_store_dwordx4 v[224:225], v[2:5], off offset:576
	s_and_b64 vcc, exec, s[0:1]
	s_mov_b32 s47, s16
	s_mov_b32 s46, s22
	s_mov_b64 s[52:53], s[44:45]
	s_mov_b64 s[48:49], s[24:25]
	v_readlane_b32 s93, v254, 9
	s_cbranch_vccz .LBB0_521
	s_waitcnt vmcnt(0)
	s_cmpk_gt_u32 s2, 0xff
	s_cbranch_scc1 .LBB0_532
	s_barrier
